# baseline (speedup 1.0000x reference)
_Z6k_gemmPKfS0_PK15HIP_vector_typeIjLj4EEPDF16_PKh:
	s_load_dwordx4 s[20:23], s[0:1], 0x0
	s_load_dwordx4 s[4:7], s[0:1], 0x10
	s_load_dwordx2 s[38:39], s[0:1], 0x20
	v_readfirstlane_b32 s8, v0
	v_and_b32_e32 v1, 63, v0
	s_nop 3
	s_lshr_b32 s8, s8, 6
	s_and_b32 s40, s2, 7
	s_lshr_b32 s41, s2, 3
	s_mul_i32 s18, s40, 0x187
	s_add_u32 s19, s18, 0x187
	s_min_u32 s19, s19, 0xc35
	s_sub_u32 s33, s19, s18
	s_sub_u32 s33, s33, 0x180
	s_lshl_b32 s33, s33, 2
	s_cmp_lt_u32 s41, s33
	s_cselect_b32 s44, 7, 6
	s_lshr_b32 s45, s41, 2
	s_add_u32 s45, s45, s18
	s_add_u32 s45, s45, 0x180
	s_lshl_b32 s45, s45, 4
	s_and_b32 s46, s41, 3
	s_lshl_b32 s46, s46, 2
	s_add_u32 s47, s45, s46
	s_mul_i32 s45, s47, 0x4b0
	s_lshl_b32 s46, s47, 8
	s_add_i32 s18, s18, s41
	s_cmp_eq_u32 s8, 0
	s_cselect_b32 s9, s44, 6
	s_add_i32 s11, s44, 4
	s_lshl_b32 s18, s18, 4
	s_lshl_b32 s19, s8, 2
	s_add_i32 s33, s18, s19
	s_mul_i32 s12, s33, 0x4b0
	s_lshl_b32 s32, s18, 8
	s_sub_u32 s32, s32, 0x100000
	s_mov_b32 s10, 0
	v_lshl_add_u32 v253, v1, 10, s33
	v_mov_b32_e32 v254, s47
	v_cmp_eq_u32_e32 vcc, 6, v1
	s_nop 1
	v_cndmask_b32_e32 v253, v253, v254, vcc
	v_mov_b32_e32 v247, 0
	v_cmp_gt_i32_e32 vcc, s9, v1
	s_mov_b32 s18, 0xc350
	v_cmp_gt_i32_e64 s[36:37], s18, v253
	s_and_b64 vcc, vcc, s[36:37]
	s_waitcnt lgkmcnt(0)
	s_and_saveexec_b64 s[36:37], vcc
	global_load_dword v247, v253, s[38:39]
	s_mov_b64 exec, s[36:37]
	s_mov_b32 s24, s22
	s_and_b32 s25, s23, 0xffff
	s_mov_b32 s26, 0x3938700
	s_mov_b32 s27, 0x20000
	s_and_b32 s21, s21, 0xffff
	s_mov_b32 s22, 0x3938700
	s_mov_b32 s23, 0x20000
	s_mov_b32 s28, s6
	s_and_b32 s29, s7, 0xffff
	s_mov_b32 s30, 0xc35000
	s_mov_b32 s31, 0x20000
	v_lshlrev_b32_e32 v238, 4, v1
	v_mul_u32_u24_e32 v253, 0x1746, v1
	v_lshrrev_b32_e32 v253, 16, v253
	v_min_u32_e32 v253, 3, v253
	v_mul_u32_u24_e32 v254, 11, v253
	v_sub_u32_e32 v254, v1, v254
	v_lshlrev_b32_e32 v240, 3, v253
	v_mul_u32_u24_e32 v249, 0x4b0, v253
	v_lshl_add_u32 v249, v254, 4, v249
	v_add_u32_e32 v249, 0x400, v249
	v_mov_b32_e32 v255, 0x80000000
	v_cmp_gt_u32_e64 s[34:35], 44, v1
	s_nop 1
	v_cndmask_b32_e64 v239, v255, v249, s[34:35]
	v_lshl_add_u32 v250, s8, 2, v253
	v_mul_u32_u24_e32 v250, 0x4e0, v250
	v_lshl_add_u32 v250, v254, 3, v250
	v_add_u32_e32 v242, 0x200, v250
	s_mul_i32 s18, s8, 0x1380
	v_lshl_add_u32 v241, v1, 3, s18
	v_and_b32_e32 v249, 15, v1
	v_lshrrev_b32_e32 v250, 4, v1
	v_mul_u32_u24_e32 v243, 0x4e0, v249
	v_lshl_add_u32 v243, v250, 4, v243
	v_mul_u32_u24_e32 v244, 0x440, v250
	v_lshl_add_u32 v244, v249, 1, v244
	s_lshl_b32 s18, s8, 6
	s_add_i32 s18, s18, 39936
	v_add_u32_e32 v244, s18, v244
	v_lshrrev_b32_e32 v249, 4, v0
	v_and_b32_e32 v250, 15, v0
	v_mul_u32_u24_e32 v245, 0x110, v249
	v_lshl_add_u32 v245, v250, 4, v245
	v_add_u32_e32 v245, 39936, v245
	v_lshlrev_b32_e32 v246, 8, v249
	v_lshl_add_u32 v246, v250, 4, v246
	s_lshl_b32 s18, s8, 12
	s_add_i32 s18, s18, 48640
	v_lshl_add_u32 v248, v1, 4, s18
	v_cmp_gt_u32_e32 vcc, 32, v0
	s_and_saveexec_b64 s[36:37], vcc
	v_mul_u32_u24_e32 v251, 0x4e00, v249
	v_mul_u32_u24_e32 v252, 0x4e0, v250
	v_add_u32_e32 v254, v251, v252
	v_mov_b32_e32 v250, 0
	v_mov_b32_e32 v251, 0
	v_mov_b32_e32 v252, 0
	v_mov_b32_e32 v253, 0
	ds_write_b128 v254, v[250:253] offset:1200
	s_mov_b64 exec, s[36:37]
	s_lshl_b32 s18, s8, 11
	v_lshl_add_u32 v253, v1, 4, s18
	v_add_u32_e32 v254, 0x22000, v253
	global_load_dwordx4 v[178:181], v254, s[4:5]
	global_load_dwordx4 v[182:185], v254, s[4:5] offset:1024
	v_add_u32_e32 v254, 0x2000, v254
	global_load_dwordx4 v[186:189], v254, s[4:5]
	global_load_dwordx4 v[190:193], v254, s[4:5] offset:1024
	v_mov_b32_e32 v236, v253
	s_waitcnt vmcnt(4)
	v_readlane_b32 s13, v247, s10
	s_add_u32 s14, s12, 0x4b0
	s_add_u32 s15, s12, 0x960
	s_add_u32 s16, s12, 0xe10
	s_nop 1
	s_and_b32 s18, s13, 0xff
	s_cmp_eq_u32 s18, 1
	s_cselect_b32 s42, s12, 0x80000000
	s_and_b32 s18, s13, 0xff00
	s_cmp_eq_u32 s18, 0x100
	s_cselect_b32 s14, s14, 0x80000000
	s_and_b32 s18, s13, 0xff0000
	s_cmp_eq_u32 s18, 0x10000
	s_cselect_b32 s15, s15, 0x80000000
	s_and_b32 s18, s13, 0xff000000
	s_cmp_eq_u32 s18, 0x1000000
	s_cselect_b32 s16, s16, 0x80000000
	v_lshrrev_b32_e64 v249, v240, s13
	v_and_b32_e32 v249, 0xff, v249
	v_cmp_eq_u32_e32 vcc, 1, v249
	s_nop 1
	v_cndmask_b32_e32 v254, v255, v239, vcc
	buffer_load_dwordx4 v[138:141], v238, s[20:23], s42 offen sc1 nt
	buffer_load_dwordx4 v[142:145], v238, s[24:27], s42 offen sc1 nt
	buffer_load_dwordx4 v[146:149], v238, s[20:23], s14 offen sc1 nt
	buffer_load_dwordx4 v[150:153], v238, s[24:27], s14 offen sc1 nt
	buffer_load_dwordx4 v[154:157], v238, s[20:23], s15 offen sc1 nt
	buffer_load_dwordx4 v[158:161], v238, s[24:27], s15 offen sc1 nt
	buffer_load_dwordx4 v[162:165], v238, s[20:23], s16 offen sc1 nt
	buffer_load_dwordx4 v[166:169], v238, s[24:27], s16 offen sc1 nt
	buffer_load_dwordx4 v[170:173], v254, s[20:23], s12 offen sc1 nt
	buffer_load_dwordx4 v[174:177], v254, s[24:27], s12 offen sc1 nt
	s_add_u32 s12, s12, 0x12c000
	s_add_u32 s32, s32, 0x40000
	s_mov_b32 s19, 0x80000000
	buffer_store_dwordx4 v[226:229], v246, s[28:31], s19 offen sc0 sc1
	s_mov_b32 s10, 1
	global_load_dwordx4 v[2:5], v236, s[4:5]
	global_load_dwordx4 v[6:9], v236, s[4:5] offset:1024
	v_add_u32_e32 v236, 0x2000, v236
	global_load_dwordx4 v[10:13], v236, s[4:5]
	global_load_dwordx4 v[14:17], v236, s[4:5] offset:1024
	v_add_u32_e32 v236, 0x2000, v236
	global_load_dwordx4 v[18:21], v236, s[4:5]
	global_load_dwordx4 v[22:25], v236, s[4:5] offset:1024
	v_add_u32_e32 v236, 0x2000, v236
	global_load_dwordx4 v[26:29], v236, s[4:5]
	global_load_dwordx4 v[30:33], v236, s[4:5] offset:1024
	v_add_u32_e32 v236, 0x2000, v236
	global_load_dwordx4 v[34:37], v236, s[4:5]
	global_load_dwordx4 v[38:41], v236, s[4:5] offset:1024
	v_add_u32_e32 v236, 0x2000, v236
	global_load_dwordx4 v[42:45], v236, s[4:5]
	global_load_dwordx4 v[46:49], v236, s[4:5] offset:1024
	v_add_u32_e32 v236, 0x2000, v236
	global_load_dwordx4 v[50:53], v236, s[4:5]
	global_load_dwordx4 v[54:57], v236, s[4:5] offset:1024
	v_add_u32_e32 v236, 0x2000, v236
	global_load_dwordx4 v[58:61], v236, s[4:5]
	global_load_dwordx4 v[62:65], v236, s[4:5] offset:1024
	v_add_u32_e32 v236, 0x2000, v236
	global_load_dwordx4 v[66:69], v236, s[4:5]
	global_load_dwordx4 v[70:73], v236, s[4:5] offset:1024
	v_add_u32_e32 v236, 0x2000, v236
	global_load_dwordx4 v[74:77], v236, s[4:5]
	global_load_dwordx4 v[78:81], v236, s[4:5] offset:1024
	v_add_u32_e32 v236, 0x2000, v236
	global_load_dwordx4 v[82:85], v236, s[4:5]
	global_load_dwordx4 v[86:89], v236, s[4:5] offset:1024
	v_add_u32_e32 v236, 0x2000, v236
	global_load_dwordx4 v[90:93], v236, s[4:5]
	global_load_dwordx4 v[94:97], v236, s[4:5] offset:1024
	v_add_u32_e32 v236, 0x2000, v236
	global_load_dwordx4 v[98:101], v236, s[4:5]
	global_load_dwordx4 v[102:105], v236, s[4:5] offset:1024
	v_add_u32_e32 v236, 0x2000, v236
	global_load_dwordx4 v[106:109], v236, s[4:5]
	global_load_dwordx4 v[110:113], v236, s[4:5] offset:1024
	v_add_u32_e32 v236, 0x2000, v236
	global_load_dwordx4 v[114:117], v236, s[4:5]
	global_load_dwordx4 v[118:121], v236, s[4:5] offset:1024
	v_add_u32_e32 v236, 0x2000, v236
	global_load_dwordx4 v[122:125], v236, s[4:5]
	global_load_dwordx4 v[126:129], v236, s[4:5] offset:1024
	v_add_u32_e32 v236, 0x2000, v236
	global_load_dwordx4 v[130:133], v236, s[4:5]
	global_load_dwordx4 v[134:137], v236, s[4:5] offset:1024
	s_waitcnt vmcnt(45)
	ds_write_b128 v248, v[178:181]
	ds_write_b128 v248, v[182:185] offset:1024
	ds_write_b128 v248, v[186:189] offset:2048
	ds_write_b128 v248, v[190:193] offset:3072
	s_waitcnt lgkmcnt(0)
	s_barrier
	s_branch .Lg_half1

.Lg_noprep0:
	s_sub_u32 s18, s10, 2
	s_cmp_lt_u32 s18, s9
	s_cbranch_scc0 .Lg_s2skip0
	s_cmp_gt_u32 s10, s9
	s_cbranch_scc1 .Lg_s2finalb0
	s_cmp_eq_u32 s10, s9
	s_cbranch_scc1 .Lg_s2final0
	s_waitcnt vmcnt(21)
	v_cvt_pk_f16_f32 v250, v138, v139
	v_cvt_pk_f16_f32 v251, v140, v141
	ds_write_b64 v241, v[250:251] offset:0
	buffer_load_dwordx4 v[138:141], v238, s[20:23], s42 offen sc1 nt
	s_waitcnt vmcnt(21)
	v_cvt_pk_f16_f32 v252, v142, v143
	v_cvt_pk_f16_f32 v253, v144, v145
	ds_write_b64 v241, v[252:253] offset:600
	buffer_load_dwordx4 v[142:145], v238, s[24:27], s42 offen sc1 nt
	s_waitcnt vmcnt(21)
	v_cvt_pk_f16_f32 v250, v146, v147
	v_cvt_pk_f16_f32 v251, v148, v149
	ds_write_b64 v241, v[250:251] offset:1248
	buffer_load_dwordx4 v[146:149], v238, s[20:23], s14 offen sc1 nt
	s_waitcnt vmcnt(21)
	v_cvt_pk_f16_f32 v252, v150, v151
	v_cvt_pk_f16_f32 v253, v152, v153
	ds_write_b64 v241, v[252:253] offset:1848
	buffer_load_dwordx4 v[150:153], v238, s[24:27], s14 offen sc1 nt
	s_waitcnt vmcnt(21)
	v_cvt_pk_f16_f32 v250, v154, v155
	v_cvt_pk_f16_f32 v251, v156, v157
	ds_write_b64 v241, v[250:251] offset:2496
	buffer_load_dwordx4 v[154:157], v238, s[20:23], s15 offen sc1 nt
	s_waitcnt vmcnt(21)
	v_cvt_pk_f16_f32 v252, v158, v159
	v_cvt_pk_f16_f32 v253, v160, v161
	ds_write_b64 v241, v[252:253] offset:3096
	buffer_load_dwordx4 v[158:161], v238, s[24:27], s15 offen sc1 nt
	s_waitcnt vmcnt(21)
	v_cvt_pk_f16_f32 v250, v162, v163
	v_cvt_pk_f16_f32 v251, v164, v165
	ds_write_b64 v241, v[250:251] offset:3744
	buffer_load_dwordx4 v[162:165], v238, s[20:23], s16 offen sc1 nt
	s_waitcnt vmcnt(21)
	v_cvt_pk_f16_f32 v252, v166, v167
	v_cvt_pk_f16_f32 v253, v168, v169
	ds_write_b64 v241, v[252:253] offset:4344
	buffer_load_dwordx4 v[166:169], v238, s[24:27], s16 offen sc1 nt
	s_mov_b64 exec, s[34:35]
	s_waitcnt vmcnt(21)
	v_cvt_pk_f16_f32 v250, v170, v171
	v_cvt_pk_f16_f32 v251, v172, v173
	ds_write_b64 v242, v[250:251] offset:0
	s_mov_b64 exec, -1
	buffer_load_dwordx4 v[170:173], v254, s[20:23], s12 offen sc1 nt
	s_mov_b64 exec, s[34:35]
	s_waitcnt vmcnt(21)
	v_cvt_pk_f16_f32 v252, v174, v175
	v_cvt_pk_f16_f32 v253, v176, v177
	ds_write_b64 v242, v[252:253] offset:600
	s_mov_b64 exec, -1
	buffer_load_dwordx4 v[174:177], v254, s[24:27], s12 offen sc1 nt
	s_branch .Lg_s1done0

.Lg_s2skip0:
	s_cmp_ge_u32 s10, s9
	s_cbranch_scc1 .Lg_s1done0
	buffer_load_dwordx4 v[138:141], v238, s[20:23], s42 offen sc1 nt
	buffer_load_dwordx4 v[142:145], v238, s[24:27], s42 offen sc1 nt
	buffer_load_dwordx4 v[146:149], v238, s[20:23], s14 offen sc1 nt
	buffer_load_dwordx4 v[150:153], v238, s[24:27], s14 offen sc1 nt
	buffer_load_dwordx4 v[154:157], v238, s[20:23], s15 offen sc1 nt
	buffer_load_dwordx4 v[158:161], v238, s[24:27], s15 offen sc1 nt
	buffer_load_dwordx4 v[162:165], v238, s[20:23], s16 offen sc1 nt
	buffer_load_dwordx4 v[166:169], v238, s[24:27], s16 offen sc1 nt
	buffer_load_dwordx4 v[170:173], v254, s[20:23], s12 offen sc1 nt
	buffer_load_dwordx4 v[174:177], v254, s[24:27], s12 offen sc1 nt

.Lg_noprep1:
	s_sub_u32 s18, s10, 2
	s_cmp_lt_u32 s18, s9
	s_cbranch_scc0 .Lg_s2skip1
	s_cmp_gt_u32 s10, s9
	s_cbranch_scc1 .Lg_s2finalb1
	s_cmp_eq_u32 s10, s9
	s_cbranch_scc1 .Lg_s2final1
	s_waitcnt vmcnt(21)
	v_cvt_pk_f16_f32 v250, v178, v179
	v_cvt_pk_f16_f32 v251, v180, v181
	ds_write_b64 v241, v[250:251] offset:19968
	buffer_load_dwordx4 v[178:181], v238, s[20:23], s42 offen sc1 nt
	s_waitcnt vmcnt(21)
	v_cvt_pk_f16_f32 v252, v182, v183
	v_cvt_pk_f16_f32 v253, v184, v185
	ds_write_b64 v241, v[252:253] offset:20568
	buffer_load_dwordx4 v[182:185], v238, s[24:27], s42 offen sc1 nt
	s_waitcnt vmcnt(21)
	v_cvt_pk_f16_f32 v250, v186, v187
	v_cvt_pk_f16_f32 v251, v188, v189
	ds_write_b64 v241, v[250:251] offset:21216
	buffer_load_dwordx4 v[186:189], v238, s[20:23], s14 offen sc1 nt
	s_waitcnt vmcnt(21)
	v_cvt_pk_f16_f32 v252, v190, v191
	v_cvt_pk_f16_f32 v253, v192, v193
	ds_write_b64 v241, v[252:253] offset:21816
	buffer_load_dwordx4 v[190:193], v238, s[24:27], s14 offen sc1 nt
	s_waitcnt vmcnt(21)
	v_cvt_pk_f16_f32 v250, v194, v195
	v_cvt_pk_f16_f32 v251, v196, v197
	ds_write_b64 v241, v[250:251] offset:22464
	buffer_load_dwordx4 v[194:197], v238, s[20:23], s15 offen sc1 nt
	s_waitcnt vmcnt(21)
	v_cvt_pk_f16_f32 v252, v198, v199
	v_cvt_pk_f16_f32 v253, v200, v201
	ds_write_b64 v241, v[252:253] offset:23064
	buffer_load_dwordx4 v[198:201], v238, s[24:27], s15 offen sc1 nt
	s_waitcnt vmcnt(21)
	v_cvt_pk_f16_f32 v250, v202, v203
	v_cvt_pk_f16_f32 v251, v204, v205
	ds_write_b64 v241, v[250:251] offset:23712
	buffer_load_dwordx4 v[202:205], v238, s[20:23], s16 offen sc1 nt
	s_waitcnt vmcnt(21)
	v_cvt_pk_f16_f32 v252, v206, v207
	v_cvt_pk_f16_f32 v253, v208, v209
	ds_write_b64 v241, v[252:253] offset:24312
	buffer_load_dwordx4 v[206:209], v238, s[24:27], s16 offen sc1 nt
	s_mov_b64 exec, s[34:35]
	s_waitcnt vmcnt(21)
	v_cvt_pk_f16_f32 v250, v210, v211
	v_cvt_pk_f16_f32 v251, v212, v213
	ds_write_b64 v242, v[250:251] offset:19968
	s_mov_b64 exec, -1
	buffer_load_dwordx4 v[210:213], v254, s[20:23], s12 offen sc1 nt
	s_mov_b64 exec, s[34:35]
	s_waitcnt vmcnt(21)
	v_cvt_pk_f16_f32 v252, v214, v215
	v_cvt_pk_f16_f32 v253, v216, v217
	ds_write_b64 v242, v[252:253] offset:20568
	s_mov_b64 exec, -1
	buffer_load_dwordx4 v[214:217], v254, s[24:27], s12 offen sc1 nt
	s_branch .Lg_s1done1

.Lg_s2skip1:
	s_cmp_ge_u32 s10, s9
	s_cbranch_scc1 .Lg_s1done1
	buffer_load_dwordx4 v[178:181], v238, s[20:23], s42 offen sc1 nt
	buffer_load_dwordx4 v[182:185], v238, s[24:27], s42 offen sc1 nt
	buffer_load_dwordx4 v[186:189], v238, s[20:23], s14 offen sc1 nt
	buffer_load_dwordx4 v[190:193], v238, s[24:27], s14 offen sc1 nt
	buffer_load_dwordx4 v[194:197], v238, s[20:23], s15 offen sc1 nt
	buffer_load_dwordx4 v[198:201], v238, s[24:27], s15 offen sc1 nt
	buffer_load_dwordx4 v[202:205], v238, s[20:23], s16 offen sc1 nt
	buffer_load_dwordx4 v[206:209], v238, s[24:27], s16 offen sc1 nt
	buffer_load_dwordx4 v[210:213], v254, s[20:23], s12 offen sc1 nt
	buffer_load_dwordx4 v[214:217], v254, s[24:27], s12 offen sc1 nt
